# baseline (speedup 1.0000x reference)
_Z7k_fine3PKfS0_PKtS2_PKdS4_S0_PiPfS5_S0_S0_PtS7_:
	s_load_dwordx2 s[4:5], s[0:1], 0x30
	s_load_dwordx8 s[68:75], s[0:1], 0x0
	s_load_dwordx2 s[88:89], s[0:1], 0x48
	s_load_dwordx4 s[80:83], s[0:1], 0x20
	s_load_dwordx8 s[60:67], s[0:1], 0x50
	s_lshl_b32 s3, s2, 5
	s_and_b32 s3, s3, 0xe0
	s_lshr_b32 s76, s2, 3
	s_add_i32 s3, s3, s76
	s_lshr_b32 s84, s3, 1
	s_mov_b32 s85, 0
	s_lshl_b64 s[6:7], s[84:85], 14
	s_waitcnt lgkmcnt(0)
	s_add_u32 s4, s4, s6
	s_addc_u32 s5, s5, s7
	v_lshlrev_b32_e32 v2, 2, v0
	v_mov_b32_e32 v3, 0
	v_lshl_add_u64 v[4:5], s[4:5], 0, v[2:3]
	s_mov_b32 s6, 0x200000
	v_add_co_u32_e32 v6, vcc, s6, v4
	s_mov_b32 s7, 0x400000
	s_nop 0
	v_addc_co_u32_e32 v7, vcc, 0, v5, vcc
	v_or_b32_e32 v117, 0x400, v0
	v_add_co_u32_e32 v8, vcc, s7, v4
	v_lshlrev_b32_e32 v10, 2, v117
	v_mov_b32_e32 v11, v3
	v_addc_co_u32_e32 v9, vcc, 0, v5, vcc
	v_lshl_add_u64 v[12:13], s[4:5], 0, v[10:11]
	v_add_co_u32_e32 v14, vcc, s6, v12
	s_movk_i32 s8, 0x1000
	s_nop 0
	v_addc_co_u32_e32 v15, vcc, 0, v13, vcc
	v_add_co_u32_e32 v12, vcc, s7, v12
	v_or_b32_e32 v118, 0x800, v0
	s_nop 0
	v_addc_co_u32_e32 v13, vcc, 0, v13, vcc
	v_add_co_u32_e32 v16, vcc, s8, v4
	s_mov_b32 s8, 0x201000
	s_nop 0
	v_addc_co_u32_e32 v17, vcc, 0, v5, vcc
	v_add_co_u32_e32 v18, vcc, s8, v4
	s_mov_b32 s8, 0x401000
	s_nop 0
	v_addc_co_u32_e32 v19, vcc, 0, v5, vcc
	global_load_dword v24, v[6:7], off nt
	global_load_dword v25, v[8:9], off nt
	global_load_dword v26, v[8:9], off offset:2048 nt
	global_load_dword v27, v[14:15], off nt
	global_load_dword v28, v[12:13], off nt
	global_load_dword v29, v[16:17], off offset:2048 nt
	global_load_dword v30, v[18:19], off offset:2048 nt
	global_load_dword v31, v[6:7], off offset:2048 nt
	v_add_co_u32_e32 v6, vcc, s8, v4
	v_lshlrev_b32_e32 v8, 2, v118
	v_mov_b32_e32 v9, v3
	v_addc_co_u32_e32 v7, vcc, 0, v5, vcc
	v_lshl_add_u64 v[12:13], s[4:5], 0, v[8:9]
	global_load_dword v32, v2, s[4:5] nt
	global_load_dword v33, v2, s[4:5] offset:2048 nt
	global_load_dword v34, v10, s[4:5] nt
	global_load_dword v35, v8, s[4:5] nt
	v_add_co_u32_e32 v8, vcc, s6, v12
	s_movk_i32 s8, 0x2000
	s_nop 0
	v_addc_co_u32_e32 v9, vcc, 0, v13, vcc
	v_add_co_u32_e32 v10, vcc, s7, v12
	v_or_b32_e32 v1, 0xc00, v0
	s_nop 0
	v_addc_co_u32_e32 v11, vcc, 0, v13, vcc
	v_add_co_u32_e32 v12, vcc, s8, v4
	s_mov_b32 s8, 0x202000
	s_nop 0
	v_addc_co_u32_e32 v13, vcc, 0, v5, vcc
	v_add_co_u32_e32 v14, vcc, s8, v4
	s_mov_b32 s8, 0x402000
	s_nop 0
	v_addc_co_u32_e32 v15, vcc, 0, v5, vcc
	v_add_co_u32_e32 v16, vcc, s8, v4
	v_lshlrev_b32_e32 v18, 2, v1
	v_mov_b32_e32 v19, v3
	v_addc_co_u32_e32 v17, vcc, 0, v5, vcc
	v_lshl_add_u64 v[20:21], s[4:5], 0, v[18:19]
	v_add_co_u32_e32 v22, vcc, s6, v20
	s_movk_i32 s6, 0x3000
	s_nop 0
	v_addc_co_u32_e32 v23, vcc, 0, v21, vcc
	v_add_co_u32_e32 v20, vcc, s7, v20
	v_and_b32_e32 v124, 63, v0
	s_nop 0
	v_addc_co_u32_e32 v21, vcc, 0, v21, vcc
	global_load_dword v3, v[6:7], off offset:2048 nt
	global_load_dword v19, v[8:9], off nt
	global_load_dword v36, v[10:11], off nt
	global_load_dword v37, v[12:13], off offset:2048 nt
	global_load_dword v38, v[14:15], off offset:2048 nt
	global_load_dword v39, v[16:17], off offset:2048 nt
	global_load_dword v40, v[22:23], off nt
	global_load_dword v41, v[20:21], off nt
	v_add_co_u32_e32 v6, vcc, s6, v4
	s_mov_b32 s6, 0x203000
	s_nop 0
	v_addc_co_u32_e32 v7, vcc, 0, v5, vcc
	v_add_co_u32_e32 v8, vcc, s6, v4
	s_mov_b32 s6, 0x403000
	s_nop 0
	v_addc_co_u32_e32 v9, vcc, 0, v5, vcc
	v_add_co_u32_e32 v4, vcc, s6, v4
	v_lshrrev_b32_e32 v116, 6, v0
	s_nop 0
	v_addc_co_u32_e32 v5, vcc, 0, v5, vcc
	global_load_dword v13, v18, s[4:5] nt
	global_load_dword v14, v[6:7], off offset:2048 nt
	global_load_dword v15, v[8:9], off offset:2048 nt
	global_load_dword v16, v[4:5], off offset:2048 nt
	s_and_b32 s90, s84, 56
	s_lshl_b32 s91, s84, 3
	s_and_b32 s91, s91, 56
	s_or_b32 s90, s90, 4
	s_or_b32 s91, s91, 4
	s_lshr_b32 s92, s3, 7
	s_lshl_b32 s92, s92, 12
	v_lshrrev_b32_e32 v152, 5, v0
	v_mul_u32_u24_e32 v153, 57, v152
	v_lshrrev_b32_e32 v153, 9, v153
	v_mad_i32_i24 v152, v153, -9, v152
	v_add_u32_e32 v154, 1, v153
	v_mul_u32_u24_e32 v153, 0xab, v152
	v_lshrrev_b32_e32 v153, 9, v153
	v_mad_i32_i24 v152, v153, -3, v152
	v_add_u32_e32 v153, -1, v153
	v_add_u32_e32 v152, -1, v152
	v_mad_i32_i24 v153, v153, v154, s90
	v_mad_i32_i24 v152, v152, v154, s91
	v_lshl_add_u32 v153, v153, 6, v152
	v_add_u32_e32 v153, s92, v153
	v_and_b32_e32 v152, 31, v0
	v_lshlrev_b32_e32 v153, 9, v153
	v_lshl_add_u32 v153, v152, 4, v153
	global_load_dwordx4 v[156:159], v153, s[68:69]
	v_add_u32_e32 v155, 0x200, v0
	v_min_u32_e32 v155, 0x35f, v155
	v_lshrrev_b32_e32 v152, 5, v155
	v_mul_u32_u24_e32 v153, 57, v152
	v_lshrrev_b32_e32 v153, 9, v153
	v_mad_i32_i24 v152, v153, -9, v152
	v_add_u32_e32 v154, 1, v153
	v_mul_u32_u24_e32 v153, 0xab, v152
	v_lshrrev_b32_e32 v153, 9, v153
	v_mad_i32_i24 v152, v153, -3, v152
	v_add_u32_e32 v153, -1, v153
	v_add_u32_e32 v152, -1, v152
	v_mad_i32_i24 v153, v153, v154, s90
	v_mad_i32_i24 v152, v152, v154, s91
	v_lshl_add_u32 v153, v153, 6, v152
	v_add_u32_e32 v153, s92, v153
	v_and_b32_e32 v152, 31, v155
	v_lshlrev_b32_e32 v153, 9, v153
	v_lshl_add_u32 v153, v152, 4, v153
	global_load_dwordx4 v[160:163], v153, s[68:69]
	s_lshl_b32 s93, s90, 6
	s_add_i32 s93, s93, s91
	s_add_i32 s93, s93, s92
	s_lshl_b32 s93, s93, 3
	v_subrev_u32_e32 v165, 63, v0
	v_max_i32_e32 v165, 1, v165
	v_min_i32_e32 v165, 3, v165
	v_mul_u32_u24_e32 v166, 0x208, v165
	v_mul_u32_u24_e32 v167, 0x1f8, v165
	v_lshlrev_b32_e32 v168, 9, v165
	v_lshlrev_b32_e32 v169, 3, v165
	v_sub_u32_e32 v170, s93, v166
	global_load_dwordx2 v[172:173], v170, s[80:81]
	v_sub_u32_e32 v170, s93, v168
	global_load_dwordx2 v[174:175], v170, s[80:81]
	v_sub_u32_e32 v170, s93, v167
	global_load_dwordx2 v[176:177], v170, s[80:81]
	v_sub_u32_e32 v170, s93, v169
	global_load_dwordx2 v[178:179], v170, s[80:81]
	v_add_u32_e32 v170, s93, v169
	global_load_dwordx2 v[180:181], v170, s[80:81]
	v_add_u32_e32 v170, s93, v167
	global_load_dwordx2 v[182:183], v170, s[80:81]
	v_add_u32_e32 v170, s93, v168
	global_load_dwordx2 v[184:185], v170, s[80:81]
	v_add_u32_e32 v170, s93, v166
	global_load_dwordx2 v[186:187], v170, s[80:81]
	s_add_u32 s94, s80, s93
	s_addc_u32 s95, s81, 0
	s_load_dwordx2 s[94:95], s[94:95], 0x0
	v_lshl_or_b32 v171, s2, 9, v0
	v_lshlrev_b32_e32 v171, 4, v171
	global_load_dwordx4 v[216:219], v171, s[62:63] nt
	v_add_u32_e32 v170, 0x200000, v171
	global_load_dwordx4 v[220:223], v170, s[62:63] nt
	v_add_u32_e32 v170, 0x400000, v171
	global_load_dwordx4 v[224:227], v170, s[62:63] nt
	v_add_u32_e32 v170, 0x600000, v171
	global_load_dwordx4 v[228:231], v170, s[62:63] nt
	s_mov_b32 s4, 0xff800000
	v_cmp_eq_u32_e64 s[42:43], 0, v124
	s_waitcnt vmcnt(29)
	v_add_f32_e32 v4, v32, v24
	v_add_f32_e32 v12, v4, v25
	s_waitcnt vmcnt(28)
	v_add_f32_e32 v4, v33, v31
	s_waitcnt vmcnt(27)
	v_add_f32_e32 v5, v34, v27
	v_add_f32_e32 v11, v4, v26
	v_add_f32_e32 v10, v5, v28
	v_add_f32_e32 v5, v29, v30
	v_max3_f32 v4, v12, s4, v11
	s_waitcnt vmcnt(25)
	v_add_f32_e32 v9, v5, v3
	v_max3_f32 v3, v4, v10, v9
	s_waitcnt vmcnt(24)
	v_add_f32_e32 v4, v35, v19
	s_waitcnt vmcnt(23)
	v_add_f32_e32 v8, v4, v36
	s_waitcnt vmcnt(21)
	v_add_f32_e32 v4, v37, v38
	v_mbcnt_lo_u32_b32 v5, -1, 0
	s_waitcnt vmcnt(20)
	v_add_f32_e32 v7, v4, v39
	v_mbcnt_hi_u32_b32 v5, -1, v5
	v_max3_f32 v4, v3, v8, v7
	s_waitcnt vmcnt(17)
	v_add_f32_e32 v3, v13, v40
	v_and_b32_e32 v13, 64, v5
	v_add_f32_e32 v6, v3, v41
	s_waitcnt vmcnt(15)
	v_add_f32_e32 v3, v14, v15
	v_add_u32_e32 v13, 64, v13
	v_xor_b32_e32 v14, 1, v5
	v_cmp_lt_i32_e32 vcc, v14, v13
	s_waitcnt vmcnt(14)
	v_add_f32_e32 v3, v3, v16
	v_max3_f32 v4, v4, v6, v3
	v_cndmask_b32_e32 v14, v5, v14, vcc
	v_lshlrev_b32_e32 v115, 2, v14
	ds_bpermute_b32 v14, v115, v4
	s_waitcnt lgkmcnt(0)
	v_max_f32_e32 v14, v14, v14
	v_max_f32_e32 v4, v4, v14
	v_xor_b32_e32 v14, 2, v5
	v_cmp_lt_i32_e32 vcc, v14, v13
	s_nop 1
	v_cndmask_b32_e32 v14, v5, v14, vcc
	v_lshlrev_b32_e32 v114, 2, v14
	ds_bpermute_b32 v14, v114, v4
	s_waitcnt lgkmcnt(0)
	v_max_f32_e32 v14, v14, v14
	v_max_f32_e32 v4, v4, v14
	v_xor_b32_e32 v14, 4, v5
	v_cmp_lt_i32_e32 vcc, v14, v13
	s_nop 1
	v_cndmask_b32_e32 v14, v5, v14, vcc
	v_lshlrev_b32_e32 v113, 2, v14
	ds_bpermute_b32 v14, v113, v4
	s_waitcnt lgkmcnt(0)
	v_max_f32_e32 v14, v14, v14
	v_max_f32_e32 v4, v4, v14
	v_xor_b32_e32 v14, 8, v5
	v_cmp_lt_i32_e32 vcc, v14, v13
	s_nop 1
	v_cndmask_b32_e32 v14, v5, v14, vcc
	v_lshlrev_b32_e32 v112, 2, v14
	ds_bpermute_b32 v14, v112, v4
	s_waitcnt lgkmcnt(0)
	v_max_f32_e32 v14, v14, v14
	v_max_f32_e32 v4, v4, v14
	v_xor_b32_e32 v14, 16, v5
	v_cmp_lt_i32_e32 vcc, v14, v13
	s_nop 1
	v_cndmask_b32_e32 v14, v5, v14, vcc
	v_lshlrev_b32_e32 v122, 2, v14
	ds_bpermute_b32 v14, v122, v4
	s_waitcnt lgkmcnt(0)
	v_max_f32_e32 v14, v14, v14
	v_max_f32_e32 v4, v4, v14
	v_xor_b32_e32 v14, 32, v5
	v_cmp_lt_i32_e32 vcc, v14, v13
	s_nop 1
	v_cndmask_b32_e32 v5, v5, v14, vcc
	v_lshlrev_b32_e32 v121, 2, v5
	ds_bpermute_b32 v5, v121, v4
	s_and_saveexec_b64 s[4:5], s[42:43]
	s_cbranch_execz .LBB2_2
	s_waitcnt lgkmcnt(0)
	v_max_f32_e32 v5, v5, v5
	v_max_f32_e32 v4, v4, v4
	v_lshl_add_u32 v13, v116, 2, 0
	v_max_f32_e32 v4, v4, v5
	ds_write_b32 v13, v4 offset:65056
.LBB2_2:
	s_or_b64 exec, exec, s[4:5]
	v_cmp_eq_u32_e32 vcc, 0, v0
	s_and_saveexec_b64 s[4:5], vcc
	v_mov_b32_e32 v4, 0
	ds_write_b32 v4, v4 offset:65088
	s_or_b64 exec, exec, s[4:5]
	s_lshl_b32 s4, s84, 3
	s_and_b32 s77, s84, 56
	s_and_b32 s33, s4, 56
	s_movk_i32 s4, 0x360
	s_lshr_b32 s86, s3, 7
	s_or_b32 s10, s77, 4
	s_or_b32 s11, s33, 4
	s_mov_b32 s87, 0
	s_lshl_b64 s[6:7], s[86:87], 12
	s_mov_b64 s[8:9], 0
	s_movk_i32 s12, 0xab
	s_movk_i32 s13, 0x15f
	v_lshlrev_b32_e32 v152, 4, v0
	s_waitcnt vmcnt(13) lgkmcnt(0)
	ds_write_b128 v152, v[156:159]
	s_movk_i32 s4, 0x160
	v_cmp_gt_u32_e32 vcc, s4, v0
	s_and_saveexec_b64 s[4:5], vcc
	s_waitcnt vmcnt(12)
	ds_write_b128 v152, v[160:163] offset:8192
	s_or_b64 exec, exec, s[4:5]
	s_load_dwordx4 s[4:7], s[0:1], 0x38
	v_subrev_u32_e32 v2, 64, v0
	v_cmp_gt_u32_e32 vcc, 3, v2
	v_lshl_add_u32 v119, v0, 3, 0
	s_waitcnt lgkmcnt(0)
	v_writelane_b32 v212, s4, 0
	s_nop 1
	v_writelane_b32 v212, s5, 1
	v_writelane_b32 v212, s6, 2
	v_writelane_b32 v212, s7, 3
	s_and_saveexec_b64 s[0:1], vcc
	s_cbranch_execz .LBB2_9
	s_mov_b32 s6, 0
	s_brev_b32 s7, 8
	v_mov_b32_e32 v2, 0x100
	v_mov_b32_e32 v13, 0xffffff80
	v_mov_b32_e32 v34, 0x260
	s_mov_b32 s4, 0x812dea11
	s_mov_b32 s5, 0x3d719799
	s_waitcnt vmcnt(4) lgkmcnt(0)
	v_add_f64 v[14:15], v[172:173], 0
	v_add_f64 v[14:15], v[14:15], v[174:175]
	v_add_f64 v[14:15], v[14:15], v[176:177]
	v_add_f64 v[14:15], v[14:15], v[178:179]
	v_add_f64 v[14:15], v[14:15], s[94:95]
	v_add_f64 v[14:15], v[14:15], v[180:181]
	v_add_f64 v[14:15], v[14:15], v[182:183]
	v_add_f64 v[14:15], v[14:15], v[184:185]
	v_add_f64 v[4:5], v[14:15], v[186:187]
	v_cmp_gt_f64_e32 vcc, s[6:7], v[4:5]
	s_nop 1
	v_cndmask_b32_e32 v2, 0, v2, vcc
	v_ldexp_f64 v[4:5], v[4:5], v2
	v_rsq_f64_e32 v[14:15], v[4:5]
	v_cndmask_b32_e32 v2, 0, v13, vcc
	v_cmp_class_f64_e32 vcc, v[4:5], v34
	v_mul_f64 v[16:17], v[4:5], v[14:15]
	v_mul_f64 v[14:15], v[14:15], 0.5
	v_fma_f64 v[18:19], -v[14:15], v[16:17], 0.5
	v_fmac_f64_e32 v[16:17], v[16:17], v[18:19]
	v_fmac_f64_e32 v[14:15], v[14:15], v[18:19]
	v_fma_f64 v[18:19], -v[16:17], v[16:17], v[4:5]
	v_fmac_f64_e32 v[16:17], v[18:19], v[14:15]
	v_fma_f64 v[18:19], -v[16:17], v[16:17], v[4:5]
	v_fmac_f64_e32 v[16:17], v[18:19], v[14:15]
	v_ldexp_f64 v[14:15], v[16:17], v2
	v_cndmask_b32_e32 v5, v15, v5, vcc
	v_cndmask_b32_e32 v4, v14, v4, vcc
	v_max_f64 v[4:5], v[4:5], s[4:5]
	v_div_scale_f64 v[14:15], s[4:5], v[4:5], v[4:5], 1.0
	v_rcp_f64_e32 v[16:17], v[14:15]
	v_div_scale_f64 v[18:19], vcc, 1.0, v[4:5], 1.0
	v_fma_f64 v[20:21], -v[14:15], v[16:17], 1.0
	v_fmac_f64_e32 v[16:17], v[16:17], v[20:21]
	v_fma_f64 v[20:21], -v[14:15], v[16:17], 1.0
	v_fmac_f64_e32 v[16:17], v[16:17], v[20:21]
	v_mul_f64 v[20:21], v[18:19], v[16:17]
	v_fma_f64 v[14:15], -v[14:15], v[20:21], v[18:19]
	v_div_fmas_f64 v[14:15], v[14:15], v[16:17], v[20:21]
	v_div_fixup_f64 v[4:5], v[14:15], v[4:5], 1.0
	ds_write_b64 v119, v[4:5] offset:64512

.LBB2_110:
	s_or_b64 exec, exec, s[0:1]
	v_bfe_u32 v65, v0, 6, 1
	v_bfe_u32 v1, v0, 3, 1
	v_lshl_or_b32 v46, v65, 1, v1
	v_lshrrev_b32_e32 v1, 3, v0
	v_and_b32_e32 v97, 15, v0
	v_and_b32_e32 v1, 48, v1
	v_or_b32_e32 v63, v1, v97
	v_mul_lo_u16_e32 v2, 20, v63
	v_lshrrev_b16_e32 v2, 7, v2
	v_and_b32_e32 v2, 14, v2
	v_or_b32_e32 v110, 64, v63
	v_add_u32_sdwa v6, v63, v2 dst_sel:DWORD dst_unused:UNUSED_PAD src0_sel:DWORD src1_sel:WORD_0
	v_mul_lo_u16_e32 v2, 0x4f, v110
	v_lshrrev_b16_e32 v2, 9, v2
	v_and_b32_e32 v2, 62, v2
	v_bfe_u32 v62, v0, 4, 2
	v_and_b32_e32 v47, 7, v0
	v_add_u32_e32 v10, v110, v2
	v_lshl_add_u32 v84, v62, 4, 0
	v_mad_u32_u24 v2, v46, 10, v47
	s_movk_i32 s0, 0x110
	s_waitcnt vmcnt(0)
	v_mad_u32_u24 v34, v2, s0, v84
	s_waitcnt lgkmcnt(0)
	s_barrier
	ds_read_b128 v[2:5], v34 offset:61200
	v_or_b32_e32 v64, 0x80, v63
	v_min_u32_e32 v22, 0xa8, v64
	v_mul_lo_u16_e32 v7, 0x4f, v22
	v_mad_u32_u24 v98, v6, s0, v84
	v_lshrrev_b16_e32 v23, 9, v7
	ds_read_b128 v[6:9], v98
	v_mad_u32_u24 v111, v10, s0, v84
	ds_read_b128 v[10:13], v111
	ds_read_b128 v[14:17], v34 offset:61264
	ds_read_b128 v[18:21], v98 offset:64
	v_and_b32_e32 v23, 30, v23
	s_waitcnt lgkmcnt(3)
	v_mfma_f32_16x16x32_f16 v[6:9], v[2:5], v[6:9], 0
	v_add_u32_e32 v26, v22, v23
	v_mad_u32_u24 v117, v26, s0, v84
	ds_read_b128 v[22:25], v111 offset:64
	ds_read_b128 v[26:29], v117
	ds_read_b128 v[30:33], v117 offset:64
	s_waitcnt lgkmcnt(3)
	v_mfma_f32_16x16x32_f16 v[6:9], v[14:17], v[18:21], v[6:9]
	ds_read_b128 v[18:21], v34 offset:61328
	v_add_u32_e32 v58, 1, v47
	v_add_u32_e32 v85, 2, v47
	v_mfma_f32_16x16x32_f16 v[10:13], v[2:5], v[10:13], 0
	v_lshl_or_b32 v86, s2, 9, v0
	v_ashrrev_i32_e32 v87, 31, v86
	v_lshlrev_b64 v[74:75], 4, v[86:87]
	s_waitcnt lgkmcnt(2)
	v_mfma_f32_16x16x32_f16 v[2:5], v[2:5], v[26:29], 0
	v_mad_u32_u24 v90, v46, 10, 20
	v_lshl_add_u64 v[70:71], s[60:61], 0, v[74:75]
	v_add_co_u32_e32 v42, vcc, 0x200000, v70
	v_mfma_f32_16x16x32_f16 v[10:13], v[14:17], v[22:25], v[10:13]
	s_nop 0
	v_addc_co_u32_e32 v43, vcc, 0, v71, vcc
	v_add_co_u32_e32 v50, vcc, 0x400000, v70
	s_waitcnt lgkmcnt(1)
	v_mfma_f32_16x16x32_f16 v[2:5], v[14:17], v[30:33], v[2:5]
	ds_read_b128 v[14:17], v98 offset:128
	ds_read_b128 v[22:25], v34 offset:61392
	ds_read_b128 v[26:29], v98 offset:192
	v_addc_co_u32_e32 v51, vcc, 0, v71, vcc
	s_waitcnt lgkmcnt(2)
	v_mfma_f32_16x16x32_f16 v[6:9], v[18:21], v[14:17], v[6:9]
	ds_read_b128 v[14:17], v111 offset:128
	ds_read_b128 v[30:33], v111 offset:192
	v_add_co_u32_e32 v52, vcc, 0x600000, v70
	s_waitcnt lgkmcnt(1)
	v_mfma_f32_16x16x32_f16 v[10:13], v[18:21], v[14:17], v[10:13]
	ds_read_b128 v[14:17], v117 offset:128
	ds_read_b128 v[34:37], v117 offset:192
	v_addc_co_u32_e32 v53, vcc, 0, v71, vcc
	s_waitcnt lgkmcnt(1)
	v_mfma_f32_16x16x32_f16 v[2:5], v[18:21], v[14:17], v[2:5]
	v_mad_u32_u24 v14, v46, 10, v58
	v_mad_u32_u24 v38, v14, s0, v84
	ds_read_b128 v[14:17], v38 offset:61200
	v_mfma_f32_16x16x32_f16 v[6:9], v[22:25], v[26:29], v[6:9]
	v_add_co_u32_e32 v54, vcc, 0x800000, v70
	s_mov_b32 s1, 0x200000
	v_mfma_f32_16x16x32_f16 v[10:13], v[22:25], v[30:33], v[10:13]
	v_addc_co_u32_e32 v55, vcc, 0, v71, vcc
	v_lshl_add_u64 v[82:83], s[62:63], 0, v[74:75]
	s_waitcnt lgkmcnt(1)
	v_mfma_f32_16x16x32_f16 v[2:5], v[22:25], v[34:37], v[2:5]
	ds_read_b128 v[18:21], v98 offset:272
	ds_read_b128 v[22:25], v38 offset:61264
	ds_read_b128 v[26:29], v98 offset:336
	s_mov_b32 s2, 0x400000
	s_mov_b32 s3, 0x600000
	s_waitcnt lgkmcnt(2)
	v_mfma_f32_16x16x32_f16 v[6:9], v[14:17], v[18:21], v[6:9]
	ds_read_b128 v[18:21], v111 offset:272
	ds_read_b128 v[30:33], v111 offset:336
	s_add_i32 s6, 0, 0x13890
	s_waitcnt lgkmcnt(1)
	v_mfma_f32_16x16x32_f16 v[10:13], v[14:17], v[18:21], v[10:13]
	ds_read_b128 v[18:21], v117 offset:272
	ds_read_b128 v[34:37], v117 offset:336
	s_waitcnt lgkmcnt(1)
	v_mfma_f32_16x16x32_f16 v[2:5], v[14:17], v[18:21], v[2:5]
	ds_read_b128 v[14:17], v38 offset:61328
	v_mfma_f32_16x16x32_f16 v[6:9], v[22:25], v[26:29], v[6:9]
	v_mfma_f32_16x16x32_f16 v[10:13], v[22:25], v[30:33], v[10:13]
	s_waitcnt lgkmcnt(1)
	v_mfma_f32_16x16x32_f16 v[2:5], v[22:25], v[34:37], v[2:5]
	ds_read_b128 v[18:21], v98 offset:400
	ds_read_b128 v[22:25], v38 offset:61392
	ds_read_b128 v[26:29], v98 offset:464
	s_waitcnt lgkmcnt(2)
	v_mfma_f32_16x16x32_f16 v[6:9], v[14:17], v[18:21], v[6:9]
	ds_read_b128 v[18:21], v111 offset:400
	ds_read_b128 v[30:33], v111 offset:464
	s_waitcnt lgkmcnt(1)
	v_mfma_f32_16x16x32_f16 v[10:13], v[14:17], v[18:21], v[10:13]
	ds_read_b128 v[18:21], v117 offset:400
	ds_read_b128 v[34:37], v117 offset:464
	s_waitcnt lgkmcnt(1)
	v_mfma_f32_16x16x32_f16 v[2:5], v[14:17], v[18:21], v[2:5]
	v_mad_u32_u24 v14, v46, 10, v85
	v_mad_u32_u24 v38, v14, s0, v84
	ds_read_b128 v[14:17], v38 offset:61200
	v_mfma_f32_16x16x32_f16 v[6:9], v[22:25], v[26:29], v[6:9]
	v_mfma_f32_16x16x32_f16 v[10:13], v[22:25], v[30:33], v[10:13]
	s_waitcnt lgkmcnt(1)
	v_mfma_f32_16x16x32_f16 v[2:5], v[22:25], v[34:37], v[2:5]
	ds_read_b128 v[18:21], v98 offset:544
	ds_read_b128 v[22:25], v38 offset:61264
	ds_read_b128 v[26:29], v98 offset:608
	s_waitcnt lgkmcnt(2)
	v_mfma_f32_16x16x32_f16 v[6:9], v[14:17], v[18:21], v[6:9]
	ds_read_b128 v[18:21], v111 offset:544
	ds_read_b128 v[30:33], v111 offset:608
	s_waitcnt lgkmcnt(1)
	v_mfma_f32_16x16x32_f16 v[10:13], v[14:17], v[18:21], v[10:13]
	ds_read_b128 v[18:21], v117 offset:544
	ds_read_b128 v[34:37], v117 offset:608
	s_waitcnt lgkmcnt(1)
	v_mfma_f32_16x16x32_f16 v[2:5], v[14:17], v[18:21], v[2:5]
	ds_read_b128 v[14:17], v38 offset:61328
	v_mfma_f32_16x16x32_f16 v[6:9], v[22:25], v[26:29], v[6:9]
	v_mfma_f32_16x16x32_f16 v[10:13], v[22:25], v[30:33], v[10:13]
	s_waitcnt lgkmcnt(1)
	v_mfma_f32_16x16x32_f16 v[2:5], v[22:25], v[34:37], v[2:5]
	ds_read_b128 v[18:21], v98 offset:672
	ds_read_b128 v[22:25], v38 offset:61392
	ds_read_b128 v[26:29], v98 offset:736
	v_mad_u32_u24 v38, v46, 10, 10
	s_waitcnt lgkmcnt(2)
	v_mfma_f32_16x16x32_f16 v[6:9], v[14:17], v[18:21], v[6:9]
	ds_read_b128 v[18:21], v111 offset:672
	ds_read_b128 v[30:33], v111 offset:736
	s_waitcnt lgkmcnt(1)
	v_mfma_f32_16x16x32_f16 v[10:13], v[14:17], v[18:21], v[10:13]
	ds_read_b128 v[18:21], v117 offset:672
	ds_read_b128 v[34:37], v117 offset:736
	s_waitcnt lgkmcnt(1)
	v_mfma_f32_16x16x32_f16 v[2:5], v[14:17], v[18:21], v[2:5]
	v_add_u32_e32 v14, v47, v38
	v_mad_u32_u24 v39, v14, s0, v84
	ds_read_b128 v[14:17], v39 offset:61200
	v_mfma_f32_16x16x32_f16 v[6:9], v[22:25], v[26:29], v[6:9]
	v_mfma_f32_16x16x32_f16 v[10:13], v[22:25], v[30:33], v[10:13]
	s_waitcnt lgkmcnt(1)
	v_mfma_f32_16x16x32_f16 v[2:5], v[22:25], v[34:37], v[2:5]
	ds_read_b128 v[18:21], v98 offset:4080
	ds_read_b128 v[22:25], v39 offset:61264
	ds_read_b128 v[26:29], v98 offset:4144
	s_waitcnt lgkmcnt(2)
	v_mfma_f32_16x16x32_f16 v[6:9], v[14:17], v[18:21], v[6:9]
	ds_read_b128 v[18:21], v111 offset:4080
	ds_read_b128 v[30:33], v111 offset:4144
	s_waitcnt lgkmcnt(1)
	v_mfma_f32_16x16x32_f16 v[10:13], v[14:17], v[18:21], v[10:13]
	ds_read_b128 v[18:21], v117 offset:4080
	ds_read_b128 v[34:37], v117 offset:4144
	s_waitcnt lgkmcnt(1)
	v_mfma_f32_16x16x32_f16 v[2:5], v[14:17], v[18:21], v[2:5]
	ds_read_b128 v[14:17], v39 offset:61328
	v_mfma_f32_16x16x32_f16 v[6:9], v[22:25], v[26:29], v[6:9]
	v_mfma_f32_16x16x32_f16 v[10:13], v[22:25], v[30:33], v[10:13]
	s_waitcnt lgkmcnt(1)
	v_mfma_f32_16x16x32_f16 v[2:5], v[22:25], v[34:37], v[2:5]
	ds_read_b128 v[18:21], v98 offset:4208
	ds_read_b128 v[22:25], v39 offset:61392
	ds_read_b128 v[26:29], v98 offset:4272
	s_waitcnt lgkmcnt(2)
	v_mfma_f32_16x16x32_f16 v[6:9], v[14:17], v[18:21], v[6:9]
	ds_read_b128 v[18:21], v111 offset:4208
	ds_read_b128 v[30:33], v111 offset:4272
	s_waitcnt lgkmcnt(1)
	v_mfma_f32_16x16x32_f16 v[10:13], v[14:17], v[18:21], v[10:13]
	ds_read_b128 v[18:21], v117 offset:4208
	ds_read_b128 v[34:37], v117 offset:4272
	s_waitcnt lgkmcnt(1)
	v_mfma_f32_16x16x32_f16 v[2:5], v[14:17], v[18:21], v[2:5]
	v_add_u32_e32 v14, v58, v38
	v_mad_u32_u24 v39, v14, s0, v84
	ds_read_b128 v[14:17], v39 offset:61200
	v_mfma_f32_16x16x32_f16 v[6:9], v[22:25], v[26:29], v[6:9]
	v_mfma_f32_16x16x32_f16 v[10:13], v[22:25], v[30:33], v[10:13]
	s_waitcnt lgkmcnt(1)
	v_mfma_f32_16x16x32_f16 v[2:5], v[22:25], v[34:37], v[2:5]
	ds_read_b128 v[18:21], v98 offset:4352
	ds_read_b128 v[22:25], v39 offset:61264
	ds_read_b128 v[26:29], v98 offset:4416
	s_waitcnt lgkmcnt(2)
	v_mfma_f32_16x16x32_f16 v[6:9], v[14:17], v[18:21], v[6:9]
	ds_read_b128 v[18:21], v111 offset:4352
	ds_read_b128 v[30:33], v111 offset:4416
	s_waitcnt lgkmcnt(1)
	v_mfma_f32_16x16x32_f16 v[10:13], v[14:17], v[18:21], v[10:13]
	ds_read_b128 v[18:21], v117 offset:4352
	ds_read_b128 v[34:37], v117 offset:4416
	s_waitcnt lgkmcnt(1)
	v_mfma_f32_16x16x32_f16 v[2:5], v[14:17], v[18:21], v[2:5]
	ds_read_b128 v[14:17], v39 offset:61328
	v_mfma_f32_16x16x32_f16 v[6:9], v[22:25], v[26:29], v[6:9]
	v_mfma_f32_16x16x32_f16 v[10:13], v[22:25], v[30:33], v[10:13]
	s_waitcnt lgkmcnt(1)
	v_mfma_f32_16x16x32_f16 v[2:5], v[22:25], v[34:37], v[2:5]
	ds_read_b128 v[18:21], v98 offset:4480
	ds_read_b128 v[22:25], v39 offset:61392
	ds_read_b128 v[26:29], v98 offset:4544
	s_waitcnt lgkmcnt(2)
	v_mfma_f32_16x16x32_f16 v[6:9], v[14:17], v[18:21], v[6:9]
	ds_read_b128 v[18:21], v111 offset:4480
	ds_read_b128 v[30:33], v111 offset:4544
	s_waitcnt lgkmcnt(1)
	v_mfma_f32_16x16x32_f16 v[10:13], v[14:17], v[18:21], v[10:13]
	ds_read_b128 v[18:21], v117 offset:4480
	ds_read_b128 v[34:37], v117 offset:4544
	s_waitcnt lgkmcnt(1)
	v_mfma_f32_16x16x32_f16 v[2:5], v[14:17], v[18:21], v[2:5]
	v_add_u32_e32 v14, v85, v38
	v_mad_u32_u24 v38, v14, s0, v84
	ds_read_b128 v[14:17], v38 offset:61200
	v_mfma_f32_16x16x32_f16 v[6:9], v[22:25], v[26:29], v[6:9]
	v_mfma_f32_16x16x32_f16 v[10:13], v[22:25], v[30:33], v[10:13]
	s_waitcnt lgkmcnt(1)
	v_mfma_f32_16x16x32_f16 v[2:5], v[22:25], v[34:37], v[2:5]
	ds_read_b128 v[18:21], v98 offset:4624
	ds_read_b128 v[22:25], v38 offset:61264
	ds_read_b128 v[26:29], v98 offset:4688
	s_waitcnt lgkmcnt(2)
	v_mfma_f32_16x16x32_f16 v[6:9], v[14:17], v[18:21], v[6:9]
	ds_read_b128 v[18:21], v111 offset:4624
	ds_read_b128 v[30:33], v111 offset:4688
	s_waitcnt lgkmcnt(1)
	v_mfma_f32_16x16x32_f16 v[10:13], v[14:17], v[18:21], v[10:13]
	ds_read_b128 v[18:21], v117 offset:4624
	ds_read_b128 v[34:37], v117 offset:4688
	s_waitcnt lgkmcnt(1)
	v_mfma_f32_16x16x32_f16 v[2:5], v[14:17], v[18:21], v[2:5]
	ds_read_b128 v[14:17], v38 offset:61328
	ds_read_b128 v[18:21], v98 offset:4752
	v_mfma_f32_16x16x32_f16 v[6:9], v[22:25], v[26:29], v[6:9]
	v_mfma_f32_16x16x32_f16 v[10:13], v[22:25], v[30:33], v[10:13]
	s_waitcnt lgkmcnt(2)
	v_mfma_f32_16x16x32_f16 v[22:25], v[22:25], v[34:37], v[2:5]
	s_nop 2
	ds_read_b128 v[2:5], v111 offset:4752
	ds_read_b128 v[26:29], v38 offset:61392
	ds_read_b128 v[30:33], v98 offset:4816
	ds_read_b128 v[34:37], v117 offset:4752
	ds_read_b128 v[38:41], v111 offset:4816
	s_waitcnt lgkmcnt(5)
	v_mfma_f32_16x16x32_f16 v[18:21], v[14:17], v[18:21], v[6:9]
	s_waitcnt lgkmcnt(4)
	v_mfma_f32_16x16x32_f16 v[10:13], v[14:17], v[2:5], v[10:13]
	s_nop 0
	global_load_dwordx4 v[6:9], v[70:71], off nt
	global_load_dwordx4 v[2:5], v[42:43], off nt
	ds_read_b128 v[42:45], v117 offset:4816
	s_waitcnt lgkmcnt(2)
	v_mfma_f32_16x16x32_f16 v[14:17], v[14:17], v[34:37], v[22:25]
	s_nop 2
	v_add_u32_e32 v22, v47, v90
	v_mad_u32_u24 v56, v22, s0, v84
	ds_read_b128 v[22:25], v56 offset:61200
	v_mfma_f32_16x16x32_f16 v[18:21], v[26:29], v[30:33], v[18:21]
	ds_read_b128 v[30:33], v98 offset:8160
	s_waitcnt lgkmcnt(3)
	v_mfma_f32_16x16x32_f16 v[10:13], v[26:29], v[38:41], v[10:13]
	s_waitcnt lgkmcnt(2)
	v_mfma_f32_16x16x32_f16 v[14:17], v[26:29], v[42:45], v[14:17]
	ds_read_b128 v[26:29], v111 offset:8160
	ds_read_b128 v[34:37], v56 offset:61264
	ds_read_b128 v[38:41], v98 offset:8224
	s_waitcnt lgkmcnt(3)
	v_mfma_f32_16x16x32_f16 v[18:21], v[22:25], v[30:33], v[18:21]
	ds_read_b128 v[30:33], v117 offset:8160
	ds_read_b128 v[42:45], v111 offset:8224
	ds_read_b128 v[46:49], v117 offset:8224
	s_waitcnt lgkmcnt(5)
	v_mfma_f32_16x16x32_f16 v[26:29], v[22:25], v[26:29], v[10:13]
	s_waitcnt lgkmcnt(2)
	v_mfma_f32_16x16x32_f16 v[22:25], v[22:25], v[30:33], v[14:17]
	s_nop 2
	global_load_dwordx4 v[14:17], v[50:51], off nt
	global_load_dwordx4 v[10:13], v[52:53], off nt
	ds_read_b128 v[30:33], v56 offset:61328
	v_mfma_f32_16x16x32_f16 v[18:21], v[34:37], v[38:41], v[18:21]
	ds_read_b128 v[38:41], v98 offset:8288
	s_waitcnt lgkmcnt(3)
	v_mfma_f32_16x16x32_f16 v[26:29], v[34:37], v[42:45], v[26:29]
	s_waitcnt lgkmcnt(2)
	v_mfma_f32_16x16x32_f16 v[22:25], v[34:37], v[46:49], v[22:25]
	ds_read_b128 v[34:37], v111 offset:8288
	ds_read_b128 v[42:45], v56 offset:61392
	ds_read_b128 v[46:49], v98 offset:8352
	v_add_co_u32_e32 v56, vcc, 0xa00000, v70
	s_waitcnt lgkmcnt(3)
	v_mfma_f32_16x16x32_f16 v[38:41], v[30:33], v[38:41], v[18:21]
	s_nop 2
	ds_read_b128 v[18:21], v117 offset:8288
	ds_read_b128 v[50:53], v111 offset:8352
	v_addc_co_u32_e32 v57, vcc, 0, v71, vcc
	s_waitcnt lgkmcnt(2)
	v_mfma_f32_16x16x32_f16 v[38:41], v[42:45], v[46:49], v[38:41]
	v_add_u32_e32 v46, v58, v90
	v_mad_u32_u24 v80, v46, s0, v84
	v_add_co_u32_e32 v76, vcc, 0xc00000, v70
	v_mfma_f32_16x16x32_f16 v[26:29], v[30:33], v[34:37], v[26:29]
	ds_read_b128 v[34:37], v117 offset:8352
	v_addc_co_u32_e32 v77, vcc, 0, v71, vcc
	s_waitcnt lgkmcnt(2)
	v_mfma_f32_16x16x32_f16 v[30:33], v[30:33], v[18:21], v[22:25]
	s_nop 2
	global_load_dwordx4 v[22:25], v[54:55], off nt
	global_load_dwordx4 v[18:21], v[56:57], off nt
	ds_read_b128 v[46:49], v80 offset:61200
	v_add_co_u32_e32 v78, vcc, 0xe00000, v70
	s_waitcnt lgkmcnt(2)
	v_mfma_f32_16x16x32_f16 v[26:29], v[42:45], v[50:53], v[26:29]
	ds_read_b128 v[50:53], v98 offset:8432
	v_addc_co_u32_e32 v79, vcc, 0, v71, vcc
	s_waitcnt lgkmcnt(2)
	v_mfma_f32_16x16x32_f16 v[30:33], v[42:45], v[34:37], v[30:33]
	ds_read_b128 v[34:37], v111 offset:8432
	ds_read_b128 v[42:45], v80 offset:61264
	ds_read_b128 v[54:57], v98 offset:8496
	v_add_co_u32_e32 v74, vcc, s1, v82
	s_waitcnt lgkmcnt(3)
	v_mfma_f32_16x16x32_f16 v[38:41], v[46:49], v[50:53], v[38:41]
	ds_read_b128 v[50:53], v117 offset:8432
	ds_read_b128 v[58:61], v111 offset:8496
	ds_read_b128 v[70:73], v117 offset:8496
	v_addc_co_u32_e32 v75, vcc, 0, v83, vcc
	s_waitcnt lgkmcnt(5)
	v_mfma_f32_16x16x32_f16 v[66:69], v[46:49], v[34:37], v[26:29]
	global_load_dwordx4 v[34:37], v[76:77], off nt
	s_nop 1
	global_load_dwordx4 v[26:29], v[78:79], off nt
	v_add_co_u32_e32 v88, vcc, s2, v82
	s_waitcnt lgkmcnt(2)
	v_mfma_f32_16x16x32_f16 v[30:33], v[46:49], v[50:53], v[30:33]
	ds_read_b128 v[46:49], v80 offset:61328
	v_addc_co_u32_e32 v89, vcc, 0, v83, vcc
	v_mfma_f32_16x16x32_f16 v[38:41], v[42:45], v[54:57], v[38:41]
	ds_read_b128 v[54:57], v98 offset:8560
	s_movk_i32 s2, 0xa9
	s_waitcnt lgkmcnt(3)
	v_mfma_f32_16x16x32_f16 v[50:53], v[42:45], v[58:61], v[66:69]
	s_waitcnt lgkmcnt(2)
	v_mfma_f32_16x16x32_f16 v[42:45], v[42:45], v[70:73], v[30:33]
	ds_read_b128 v[58:61], v111 offset:8560
	ds_read_b128 v[66:69], v80 offset:61392
	ds_read_b128 v[70:73], v98 offset:8624
	s_waitcnt lgkmcnt(3)
	v_mfma_f32_16x16x32_f16 v[54:57], v[46:49], v[54:57], v[38:41]
	s_nop 2
	ds_read_b128 v[74:77], v117 offset:8560
	ds_read_b128 v[78:81], v111 offset:8624
	s_waitcnt lgkmcnt(4)
	v_mfma_f32_16x16x32_f16 v[50:53], v[46:49], v[58:61], v[50:53]
	ds_read_b128 v[58:61], v117 offset:8624
	s_waitcnt lgkmcnt(2)
	v_mfma_f32_16x16x32_f16 v[42:45], v[46:49], v[74:77], v[42:45]
	v_mfma_f32_16x16x32_f16 v[46:49], v[66:69], v[70:73], v[54:57]
	ds_read_b128 v[70:73], v98 offset:8704
	s_nop 1
	v_add_u32_e32 v54, v85, v90
	v_mad_u32_u24 v92, v54, s0, v84
	ds_read_b128 v[54:57], v92 offset:61200
	s_waitcnt lgkmcnt(3)
	v_mfma_f32_16x16x32_f16 v[50:53], v[66:69], v[78:81], v[50:53]
	v_add_co_u32_e32 v90, vcc, s3, v82
	s_add_i32 s0, 0, 0x13550
	s_waitcnt lgkmcnt(2)
	v_mfma_f32_16x16x32_f16 v[58:61], v[66:69], v[58:61], v[42:45]
	s_nop 2
	ds_read_b128 v[42:45], v111 offset:8704
	ds_read_b128 v[66:69], v92 offset:61264
	ds_read_b128 v[74:77], v98 offset:8768
	v_addc_co_u32_e32 v91, vcc, 0, v83, vcc
	s_waitcnt lgkmcnt(3)
	v_mfma_f32_16x16x32_f16 v[70:73], v[54:57], v[70:73], v[46:49]
	ds_read_b128 v[78:81], v117 offset:8704
	ds_read_b128 v[82:85], v111 offset:8768
	v_cmp_gt_u32_e64 s[2:3], s2, v64
	v_cmp_eq_u32_e32 vcc, 0, v97
	s_waitcnt lgkmcnt(4)
	v_mfma_f32_16x16x32_f16 v[50:53], v[54:57], v[42:45], v[50:53]
	ds_read_b128 v[88:91], v117 offset:8768
	s_waitcnt lgkmcnt(2)
	v_mfma_f32_16x16x32_f16 v[54:57], v[54:57], v[78:81], v[58:61]
	s_nop 2
	ds_read_b128 v[58:61], v92 offset:61328
	ds_read_b128 v[92:95], v92 offset:61392
	ds_read_b128 v[78:81], v98 offset:8832
	ds_read_b128 v[98:101], v98 offset:8896
	ds_read_b128 v[106:109], v111 offset:8832
	ds_read_b128 v[118:121], v111 offset:8896
	ds_read_b128 v[122:125], v117 offset:8832
	ds_read_b128 v[126:129], v117 offset:8896
	v_mfma_f32_16x16x32_f16 v[102:105], v[66:69], v[74:77], v[70:73]
	s_waitcnt lgkmcnt(9)
	v_mfma_f32_16x16x32_f16 v[50:53], v[66:69], v[82:85], v[50:53]
	s_nop 0
	v_lshlrev_b32_e32 v70, 2, v62
	v_lshl_or_b32 v73, v65, 4, v70
	v_lshl_add_u32 v75, v73, 2, 0
	s_waitcnt lgkmcnt(8)
	v_mfma_f32_16x16x32_f16 v[66:69], v[66:69], v[88:91], v[54:57]
	v_add_u32_e32 v65, 0x13810, v75
	v_min_u32_e32 v72, 0xaf, v64
	v_lshl_add_u32 v70, v63, 2, s0
	s_waitcnt lgkmcnt(5)
	v_mfma_f32_16x16x32_f16 v[54:57], v[58:61], v[78:81], v[102:105]
	v_lshl_add_u32 v71, v110, 2, s0
	v_lshl_add_u32 v72, v72, 2, s0
	ds_read_b32 v65, v65
	ds_read_b32 v79, v70
	ds_read_b32 v78, v71
	ds_read_b32 v77, v72
	s_waitcnt lgkmcnt(7)
	v_mfma_f32_16x16x32_f16 v[80:83], v[58:61], v[106:109], v[50:53]
	s_movk_i32 s0, 0x69
	v_cmp_gt_u32_e64 s[0:1], s0, v63
	s_waitcnt lgkmcnt(5)
	v_mfma_f32_16x16x32_f16 v[58:61], v[58:61], v[122:125], v[66:69]
	v_mfma_f32_16x16x32_f16 v[50:53], v[92:95], v[98:101], v[54:57]
	v_mfma_f32_16x16x32_f16 v[54:57], v[92:95], v[118:121], v[80:83]
	s_waitcnt lgkmcnt(4)
	v_mfma_f32_16x16x32_f16 v[58:61], v[92:95], v[126:129], v[58:61]
	s_waitcnt lgkmcnt(2)
	s_nop 3
	v_mul_f32_e32 v50, v50, v79
	v_mul_f32_e32 v76, v65, v50
	s_waitcnt lgkmcnt(1)
	v_mul_f32_e32 v50, v54, v78
	v_mul_f32_e32 v54, v65, v50
	v_mov_b32_e32 v50, 0xff800000
	v_cndmask_b32_e64 v74, v50, v54, s[0:1]
	s_waitcnt lgkmcnt(0)
	v_mul_f32_e32 v54, v58, v77
	v_mul_f32_e32 v54, v65, v54
	v_max_f32_e32 v70, 0xff800000, v76
	v_cndmask_b32_e64 v72, v50, v54, s[2:3]
	v_max3_f32 v54, v70, v74, v72
	ds_bpermute_b32 v58, v115, v54
	s_waitcnt lgkmcnt(0)
	v_max_f32_e32 v58, v58, v58
	v_max_f32_e32 v54, v54, v58
	ds_bpermute_b32 v58, v114, v54
	s_waitcnt lgkmcnt(0)
	v_max_f32_e32 v58, v58, v58
	v_max_f32_e32 v54, v54, v58
	ds_bpermute_b32 v58, v113, v54
	s_waitcnt lgkmcnt(0)
	v_max_f32_e32 v58, v58, v58
	v_max_f32_e32 v54, v54, v58
	ds_bpermute_b32 v64, v112, v54
	v_and_b32_e32 v58, 0x180, v0
	v_add_u32_e32 v58, s6, v58
	v_lshl_add_u32 v58, v73, 2, v58
	s_and_saveexec_b64 s[6:7], vcc
	s_cbranch_execz .LBB2_112
	s_waitcnt lgkmcnt(0)
	v_max_f32_e32 v64, v64, v64
	v_max_f32_e32 v54, v54, v54
	v_max_f32_e32 v54, v54, v64
	ds_write_b32 v58, v54

.LBB2_197:
	s_or_b64 exec, exec, s[0:1]
	v_lshlrev_b64 v[0:1], 3, v[86:87]
	v_lshl_add_u64 v[50:51], s[66:67], 0, v[0:1]
	v_lshl_add_u64 v[0:1], s[64:65], 0, v[0:1]
	s_waitcnt vmcnt(6)
	v_cvt_pk_f16_f32 v5, v4, v5
	v_cvt_pk_f16_f32 v4, v2, v3
	v_add_co_u32_e32 v2, vcc, 0x100000, v0
	v_cvt_pk_f16_f32 v9, v8, v9
	s_nop 0
	v_addc_co_u32_e32 v3, vcc, 0, v1, vcc
	global_store_dwordx2 v[2:3], v[4:5], off
	v_add_co_u32_e32 v4, vcc, 0x200000, v0
	s_waitcnt vmcnt(6)
	v_cvt_pk_f16_f32 v3, v16, v17
	v_cvt_pk_f16_f32 v2, v14, v15
	v_addc_co_u32_e32 v5, vcc, 0, v1, vcc
	global_store_dwordx2 v[4:5], v[2:3], off
	v_add_co_u32_e32 v4, vcc, 0x300000, v0
	s_waitcnt vmcnt(6)
	v_cvt_pk_f16_f32 v3, v12, v13
	v_cvt_pk_f16_f32 v2, v10, v11
	v_addc_co_u32_e32 v5, vcc, 0, v1, vcc
	global_store_dwordx2 v[4:5], v[2:3], off
	v_add_co_u32_e32 v4, vcc, 0x400000, v0
	s_waitcnt vmcnt(6)
	v_cvt_pk_f16_f32 v3, v24, v25
	v_cvt_pk_f16_f32 v2, v22, v23
	v_addc_co_u32_e32 v5, vcc, 0, v1, vcc
	global_store_dwordx2 v[4:5], v[2:3], off
	v_add_co_u32_e32 v4, vcc, 0x500000, v0
	s_waitcnt vmcnt(6)
	v_cvt_pk_f16_f32 v3, v20, v21
	v_cvt_pk_f16_f32 v2, v18, v19
	v_addc_co_u32_e32 v5, vcc, 0, v1, vcc
	global_store_dwordx2 v[4:5], v[2:3], off
	v_add_co_u32_e32 v4, vcc, 0x600000, v0
	v_cvt_pk_f16_f32 v8, v6, v7
	s_nop 0
	v_addc_co_u32_e32 v5, vcc, 0, v1, vcc
	global_store_dwordx2 v[0:1], v[8:9], off
	s_waitcnt vmcnt(7)
	v_cvt_pk_f16_f32 v3, v36, v37
	v_cvt_pk_f16_f32 v2, v34, v35
	v_add_co_u32_e32 v0, vcc, 0x700000, v0
	s_mov_b32 s0, 0x100000
	global_store_dwordx2 v[4:5], v[2:3], off
	s_waitcnt vmcnt(7)
	v_cvt_pk_f16_f32 v3, v28, v29
	v_cvt_pk_f16_f32 v2, v26, v27
	v_addc_co_u32_e32 v1, vcc, 0, v1, vcc
	global_store_dwordx2 v[0:1], v[2:3], off
	s_waitcnt vmcnt(11)
	v_cvt_pk_f16_f32 v1, v218, v219
	v_cvt_pk_f16_f32 v0, v216, v217
	v_add_co_u32_e32 v2, vcc, s0, v50
	s_mov_b32 s1, 0x200000
	global_store_dwordx2 v[50:51], v[0:1], off
	s_waitcnt vmcnt(11)
	v_cvt_pk_f16_f32 v1, v222, v223
	v_cvt_pk_f16_f32 v0, v220, v221
	v_addc_co_u32_e32 v3, vcc, 0, v51, vcc
	global_store_dwordx2 v[2:3], v[0:1], off
	v_add_co_u32_e32 v2, vcc, s1, v50
	s_waitcnt vmcnt(11)
	v_cvt_pk_f16_f32 v1, v226, v227
	v_cvt_pk_f16_f32 v0, v224, v225
	v_addc_co_u32_e32 v3, vcc, 0, v51, vcc
	global_store_dwordx2 v[2:3], v[0:1], off
	v_add_co_u32_e32 v2, vcc, 0x300000, v50
	s_waitcnt vmcnt(11)
	v_cvt_pk_f16_f32 v1, v230, v231
	v_cvt_pk_f16_f32 v0, v228, v229
	v_addc_co_u32_e32 v3, vcc, 0, v51, vcc
	global_store_dwordx2 v[2:3], v[0:1], off
	s_endpgm

	.amdhsa_kernel _Z7k_fine3PKfS0_PKtS2_PKdS4_S0_PiPfS5_S0_S0_PtS7_
		.amdhsa_group_segment_fixed_size 0
		.amdhsa_private_segment_fixed_size 0
		.amdhsa_kernarg_size 112
		.amdhsa_user_sgpr_count 2
		.amdhsa_user_sgpr_dispatch_ptr 0
		.amdhsa_user_sgpr_queue_ptr 0
		.amdhsa_user_sgpr_kernarg_segment_ptr 1
		.amdhsa_user_sgpr_dispatch_id 0
		.amdhsa_user_sgpr_kernarg_preload_length 0
		.amdhsa_user_sgpr_kernarg_preload_offset 0
		.amdhsa_user_sgpr_private_segment_size 0
		.amdhsa_uses_dynamic_stack 0
		.amdhsa_enable_private_segment 0
		.amdhsa_system_sgpr_workgroup_id_x 1
		.amdhsa_system_sgpr_workgroup_id_y 0
		.amdhsa_system_sgpr_workgroup_id_z 0
		.amdhsa_system_sgpr_workgroup_info 0
		.amdhsa_system_vgpr_workitem_id 0
		.amdhsa_next_free_vgpr 232
		.amdhsa_next_free_sgpr 100
		.amdhsa_accum_offset 232
		.amdhsa_reserve_vcc 1
		.amdhsa_float_round_mode_32 0
		.amdhsa_float_round_mode_16_64 0
		.amdhsa_float_denorm_mode_32 3
		.amdhsa_float_denorm_mode_16_64 3
		.amdhsa_dx10_clamp 1
		.amdhsa_ieee_mode 1
		.amdhsa_fp16_overflow 0
		.amdhsa_tg_split 0
		.amdhsa_exception_fp_ieee_invalid_op 0
		.amdhsa_exception_fp_denorm_src 0
		.amdhsa_exception_fp_ieee_div_zero 0
		.amdhsa_exception_fp_ieee_overflow 0
		.amdhsa_exception_fp_ieee_underflow 0
		.amdhsa_exception_fp_ieee_inexact 0
		.amdhsa_exception_int_div_zero 0
	.end_amdhsa_kernel

amdhsa.kernels:
  - .agpr_count:     0
    .args:
      - .actual_access:  read_only
        .address_space:  global
        .offset:         0
        .size:           8
        .value_kind:     global_buffer
      - .actual_access:  read_only
        .address_space:  global
        .offset:         8
        .size:           8
        .value_kind:     global_buffer
      - .actual_access:  write_only
        .address_space:  global
        .offset:         16
        .size:           8
        .value_kind:     global_buffer
      - .actual_access:  write_only
        .address_space:  global
        .offset:         24
        .size:           8
        .value_kind:     global_buffer
      - .actual_access:  write_only
        .address_space:  global
        .offset:         32
        .size:           8
        .value_kind:     global_buffer
      - .actual_access:  write_only
        .address_space:  global
        .offset:         40
        .size:           8
        .value_kind:     global_buffer
      - .actual_access:  write_only
        .address_space:  global
        .offset:         48
        .size:           8
        .value_kind:     global_buffer
      - .actual_access:  write_only
        .address_space:  global
        .offset:         56
        .size:           8
        .value_kind:     global_buffer
      - .actual_access:  write_only
        .address_space:  global
        .offset:         64
        .size:           8
        .value_kind:     global_buffer
    .group_segment_fixed_size: 18944
    .kernarg_segment_align: 8
    .kernarg_segment_size: 72
    .language:       OpenCL C
    .language_version:
      - 2
      - 0
    .max_flat_workgroup_size: 256
    .name:           _Z6k_prepPKfS0_PfS1_PdS2_PtS3_S3_
    .private_segment_fixed_size: 0
    .sgpr_count:     34
    .sgpr_spill_count: 0
    .symbol:         _Z6k_prepPKfS0_PfS1_PdS2_PtS3_S3_.kd
    .uniform_work_group_size: 1
    .uses_dynamic_stack: false
    .vgpr_count:     29
    .vgpr_spill_count: 0
    .wavefront_size: 64
  - .agpr_count:     16
    .args:
      - .actual_access:  read_only
        .address_space:  global
        .offset:         0
        .size:           8
        .value_kind:     global_buffer
      - .actual_access:  read_only
        .address_space:  global
        .offset:         8
        .size:           8
        .value_kind:     global_buffer
      - .actual_access:  read_only
        .address_space:  global
        .offset:         16
        .size:           8
        .value_kind:     global_buffer
      - .actual_access:  read_only
        .address_space:  global
        .offset:         24
        .size:           8
        .value_kind:     global_buffer
      - .actual_access:  write_only
        .address_space:  global
        .offset:         32
        .size:           8
        .value_kind:     global_buffer
    .group_segment_fixed_size: 256
    .kernarg_segment_align: 8
    .kernarg_segment_size: 40
    .language:       OpenCL C
    .language_version:
      - 2
      - 0
    .max_flat_workgroup_size: 256
    .name:           _Z9k_coarse2PKtS0_PKdS2_Pf
    .private_segment_fixed_size: 0
    .sgpr_count:     37
    .sgpr_spill_count: 0
    .symbol:         _Z9k_coarse2PKtS0_PKdS2_Pf.kd
    .uniform_work_group_size: 1
    .uses_dynamic_stack: false
    .vgpr_count:     132
    .vgpr_spill_count: 0
    .wavefront_size: 64
  - .agpr_count:     0
    .args:
      - .actual_access:  read_only
        .address_space:  global
        .offset:         0
        .size:           8
        .value_kind:     global_buffer
      - .actual_access:  read_only
        .address_space:  global
        .offset:         8
        .size:           8
        .value_kind:     global_buffer
      - .actual_access:  read_only
        .address_space:  global
        .offset:         16
        .size:           8
        .value_kind:     global_buffer
      - .actual_access:  read_only
        .address_space:  global
        .offset:         24
        .size:           8
        .value_kind:     global_buffer
      - .actual_access:  read_only
        .address_space:  global
        .offset:         32
        .size:           8
        .value_kind:     global_buffer
      - .actual_access:  read_only
        .address_space:  global
        .offset:         40
        .size:           8
        .value_kind:     global_buffer
      - .actual_access:  read_only
        .address_space:  global
        .offset:         48
        .size:           8
        .value_kind:     global_buffer
      - .actual_access:  write_only
        .address_space:  global
        .offset:         56
        .size:           8
        .value_kind:     global_buffer
      - .actual_access:  write_only
        .address_space:  global
        .offset:         64
        .size:           8
        .value_kind:     global_buffer
      - .actual_access:  write_only
        .address_space:  global
        .offset:         72
        .size:           8
        .value_kind:     global_buffer
      - .actual_access:  read_only
        .address_space:  global
        .offset:         80
        .size:           8
        .value_kind:     global_buffer
      - .actual_access:  read_only
        .address_space:  global
        .offset:         88
        .size:           8
        .value_kind:     global_buffer
      - .actual_access:  write_only
        .address_space:  global
        .offset:         96
        .size:           8
        .value_kind:     global_buffer
      - .actual_access:  write_only
        .address_space:  global
        .offset:         104
        .size:           8
        .value_kind:     global_buffer
    .group_segment_fixed_size: 0
    .kernarg_segment_align: 8
    .kernarg_segment_size: 112
    .language:       OpenCL C
    .language_version:
      - 2
      - 0
    .max_flat_workgroup_size: 512
    .name:           _Z7k_fine3PKfS0_PKtS2_PKdS4_S0_PiPfS5_S0_S0_PtS7_
    .private_segment_fixed_size: 0
    .sgpr_count:     106
    .sgpr_spill_count: 4
    .symbol:         _Z7k_fine3PKfS0_PKtS2_PKdS4_S0_PiPfS5_S0_S0_PtS7_.kd
    .uniform_work_group_size: 1
    .uses_dynamic_stack: false
    .vgpr_count:     232
    .vgpr_spill_count: 0
    .wavefront_size: 64
  - .agpr_count:     0
    .args:
      - .actual_access:  read_only
        .address_space:  global
        .offset:         0
        .size:           8
        .value_kind:     global_buffer
      - .actual_access:  read_only
        .address_space:  global
        .offset:         8
        .size:           8
        .value_kind:     global_buffer
      - .actual_access:  read_only
        .address_space:  global
        .offset:         16
        .size:           8
        .value_kind:     global_buffer
      - .actual_access:  read_only
        .address_space:  global
        .offset:         24
        .size:           8
        .value_kind:     global_buffer
      - .actual_access:  read_only
        .address_space:  global
        .offset:         32
        .size:           8
        .value_kind:     global_buffer
      - .actual_access:  read_only
        .address_space:  global
        .offset:         40
        .size:           8
        .value_kind:     global_buffer
      - .actual_access:  write_only
        .address_space:  global
        .offset:         48
        .size:           8
        .value_kind:     global_buffer
      - .actual_access:  write_only
        .address_space:  global
        .offset:         56
        .size:           8
        .value_kind:     global_buffer
      - .actual_access:  write_only
        .address_space:  global
        .offset:         64
        .size:           8
        .value_kind:     global_buffer
    .group_segment_fixed_size: 18512
    .kernarg_segment_align: 8
    .kernarg_segment_size: 72
    .language:       OpenCL C
    .language_version:
      - 2
      - 0
    .max_flat_workgroup_size: 256
    .name:           _Z10k_transferPKtS0_PKfPKiS2_S4_PfS5_S5_
    .private_segment_fixed_size: 0
    .sgpr_count:     34
    .sgpr_spill_count: 0
    .symbol:         _Z10k_transferPKtS0_PKfPKiS2_S4_PfS5_S5_.kd
    .uniform_work_group_size: 1
    .uses_dynamic_stack: false
    .vgpr_count:     49
    .vgpr_spill_count: 0
    .wavefront_size: 64
